# baseline (speedup 1.0000x reference)
_Z8dog_mainPKfS0_S0_S0_S0_S0_S0_Pf:
	s_load_dwordx8 s[12:19], s[0:1], 0x0
	s_load_dwordx8 s[20:27], s[0:1], 0x20
	s_and_b32 s3, s2, 7
	s_lshl_b32 s3, s3, 5
	s_lshr_b32 s4, s2, 3
	s_add_i32 s4, s3, s4
	s_and_b32 s6, s4, 3
	s_lshr_b32 s7, s4, 2
	s_mov_b32 s5, 0
	s_lshl_b64 s[8:9], s[4:5], 18
	v_and_b32_e32 v1, 63, v0
	v_lshrrev_b32_e32 v2, 6, v0
	v_and_b32_e32 v3, 31, v0
	v_lshl_or_b32 v4, v2, 5, v3
	v_lshlrev_b32_e32 v5, 2, v4
	v_lshlrev_b32_e32 v6, 4, v1
	v_lshl_or_b32 v6, v2, 12, v6
	s_waitcnt lgkmcnt(0)
	global_load_dword v20, v5, s[18:19]
	global_load_dword v21, v5, s[20:21]
	global_load_dword v22, v5, s[22:23]
	global_load_dword v23, v5, s[24:25]
	global_load_dword v24, v5, s[14:15]
	global_load_dword v25, v5, s[16:17]
	s_add_u32 s12, s12, s8
	s_addc_u32 s13, s13, s9
	global_load_dwordx4 v[128:131], v6, s[12:13] offset:0 nt
	global_load_dwordx4 v[132:135], v6, s[12:13] offset:1024 nt
	global_load_dwordx4 v[136:139], v6, s[12:13] offset:2048 nt
	global_load_dwordx4 v[140:143], v6, s[12:13] offset:3072 nt
	v_add_u32_e32 v6, 0x8000, v6
	global_load_dwordx4 v[144:147], v6, s[12:13] offset:0 nt
	global_load_dwordx4 v[148:151], v6, s[12:13] offset:1024 nt
	global_load_dwordx4 v[152:155], v6, s[12:13] offset:2048 nt
	global_load_dwordx4 v[156:159], v6, s[12:13] offset:3072 nt
	v_bfe_u32 v7, v0, 5, 1
	v_and_b32_e32 v16, 1, v0
	v_cmp_eq_u32_e64 s[30:31], 0, v16
	v_and_b32_e32 v17, 2, v0
	v_cmp_eq_u32_e64 s[32:33], 0, v17
	v_and_b32_e32 v16, 3, v0
	v_lshrrev_b32_e32 v17, 2, v1
	v_lshlrev_b32_e32 v16, 5, v16
	v_lshl_add_u32 v16, v17, 1, v16
	v_lshrrev_b32_e32 v17, 1, v2
	s_movk_i32 s10, 0x110
	v_mad_u32_u24 v16, v17, s10, v16
	v_and_b32_e32 v17, 1, v2
	v_lshl_add_u32 v14, v17, 7, v16
	v_lshlrev_b32_e32 v17, 4, v7
	v_mad_u32_u24 v15, v3, s10, v17
	s_lshl_b32 s11, s6, 5
	v_lshl_add_u32 v18, v7, 2, s11
	v_cvt_f32_u32_e32 v18, v18
	v_lshlrev_b32_e32 v19, 3, v7
	v_cvt_f32_u32_e32 v19, v19
	s_waitcnt vmcnt(8)
	v_add_f32_e32 v26, v20, v21
	v_rcp_f32_e32 v27, v20
	v_rcp_f32_e32 v28, v26
	v_sub_f32_e32 v12, v19, v22
	v_sub_f32_e32 v13, v18, v23
	v_fma_f32 v29, -v20, v27, 1.0
	v_fma_f32 v30, -v26, v28, 1.0
	v_fma_f32 v27, v29, v27, v27
	v_fma_f32 v28, v30, v28, v28
	v_mul_f32_e32 v8, 0xbf38aa3b, v27
	v_mul_f32_e32 v9, 0xbf38aa3b, v28
	v_mul_f32_e32 v29, v24, v27
	v_mul_f32_e32 v30, v25, v28
	v_mul_f32_e32 v10, 0x3e22f983, v29
	v_mul_f32_e32 v11, 0x3e22f983, v30
	s_lshl_b32 s46, s6, 6
	s_add_i32 s46, s46, s7
	s_lshl_b32 s46, s46, 10
	s_load_dword s47, s[26:27], s46
	s_getpc_b64 s[44:45]
